# P10 epilogue: clamp reads accumulators directly, dead v_mov initialisers removed, s_nop 1 after each 128-bit store for the data-register WAR rule
# speedup vs baseline: 1.0029x; 1.0029x over previous
.LBB0_1446:
	v_lshl_or_b32 v10, s28, 8, v190
	v_med3_f32 v3, v158, s64, v196
	v_med3_f32 v4, v159, s64, v196
	v_cvt_pk_fp8_f32 v2, v3, v4
	v_med3_f32 v3, v160, s64, v196
	v_med3_f32 v4, v161, s64, v196
	v_cvt_pk_fp8_f32 v2, v3, v4 op_sel:[0,0,1]
	v_med3_f32 v4, v154, s64, v196
	v_med3_f32 v5, v155, s64, v196
	v_cvt_pk_fp8_f32 v3, v4, v5
	v_med3_f32 v4, v156, s64, v196
	v_med3_f32 v5, v157, s64, v196
	v_cvt_pk_fp8_f32 v3, v4, v5 op_sel:[0,0,1]
	v_med3_f32 v5, v150, s64, v196
	v_med3_f32 v6, v151, s64, v196
	v_cvt_pk_fp8_f32 v4, v5, v6
	v_med3_f32 v5, v152, s64, v196
	v_med3_f32 v6, v153, s64, v196
	v_cvt_pk_fp8_f32 v4, v5, v6 op_sel:[0,0,1]
	v_med3_f32 v6, v146, s64, v196
	v_med3_f32 v7, v147, s64, v196
	v_cvt_pk_fp8_f32 v5, v6, v7
	v_med3_f32 v6, v148, s64, v196
	v_med3_f32 v7, v149, s64, v196
	v_cvt_pk_fp8_f32 v5, v6, v7 op_sel:[0,0,1]
	v_med3_f32 v7, v142, s64, v196
	v_med3_f32 v8, v143, s64, v196
	v_cvt_pk_fp8_f32 v6, v7, v8
	v_med3_f32 v7, v144, s64, v196
	v_med3_f32 v8, v145, s64, v196
	v_cvt_pk_fp8_f32 v6, v7, v8 op_sel:[0,0,1]
	v_med3_f32 v8, v138, s64, v196
	v_med3_f32 v9, v139, s64, v196
	v_cvt_pk_fp8_f32 v7, v8, v9
	v_med3_f32 v8, v140, s64, v196
	v_med3_f32 v9, v141, s64, v196
	v_cvt_pk_fp8_f32 v7, v8, v9 op_sel:[0,0,1]
	v_med3_f32 v9, v134, s64, v196
	v_med3_f32 v11, v135, s64, v196
	v_cvt_pk_fp8_f32 v8, v9, v11
	v_med3_f32 v9, v136, s64, v196
	v_med3_f32 v11, v137, s64, v196
	v_cvt_pk_fp8_f32 v8, v9, v11 op_sel:[0,0,1]
	v_med3_f32 v11, v130, s64, v196
	v_med3_f32 v12, v131, s64, v196
	v_cvt_pk_fp8_f32 v9, v11, v12
	v_med3_f32 v11, v132, s64, v196
	v_med3_f32 v12, v133, s64, v196
	v_cvt_pk_fp8_f32 v9, v11, v12 op_sel:[0,0,1]
	s_lshl_b32 s23, s66, 19
	v_add3_u32 v10, s23, v171, v10
	buffer_store_dwordx4 v[2:5], v10, s[4:7], 0 offen
	s_nop 1
	v_add_u32_e32 v2, 0x8000, v10
	buffer_store_dwordx4 v[6:9], v2, s[4:7], 0 offen
	s_nop 1
	v_med3_f32 v3, v126, s64, v196
	v_med3_f32 v4, v127, s64, v196
	v_cvt_pk_fp8_f32 v2, v3, v4
	v_med3_f32 v3, v128, s64, v196
	v_med3_f32 v4, v129, s64, v196
	v_cvt_pk_fp8_f32 v2, v3, v4 op_sel:[0,0,1]
	v_med3_f32 v4, v122, s64, v196
	v_med3_f32 v5, v123, s64, v196
	v_cvt_pk_fp8_f32 v3, v4, v5
	v_med3_f32 v4, v124, s64, v196
	v_med3_f32 v5, v125, s64, v196
	v_cvt_pk_fp8_f32 v3, v4, v5 op_sel:[0,0,1]
	v_med3_f32 v5, v118, s64, v196
	v_med3_f32 v6, v119, s64, v196
	v_cvt_pk_fp8_f32 v4, v5, v6
	v_med3_f32 v5, v120, s64, v196
	v_med3_f32 v6, v121, s64, v196
	v_cvt_pk_fp8_f32 v4, v5, v6 op_sel:[0,0,1]
	v_med3_f32 v6, v114, s64, v196
	v_med3_f32 v7, v115, s64, v196
	v_cvt_pk_fp8_f32 v5, v6, v7
	v_med3_f32 v6, v116, s64, v196
	v_med3_f32 v7, v117, s64, v196
	v_cvt_pk_fp8_f32 v5, v6, v7 op_sel:[0,0,1]
	v_med3_f32 v7, v110, s64, v196
	v_med3_f32 v8, v111, s64, v196
	v_cvt_pk_fp8_f32 v6, v7, v8
	v_med3_f32 v7, v112, s64, v196
	v_med3_f32 v8, v113, s64, v196
	v_cvt_pk_fp8_f32 v6, v7, v8 op_sel:[0,0,1]
	v_med3_f32 v8, v106, s64, v196
	v_med3_f32 v9, v107, s64, v196
	v_cvt_pk_fp8_f32 v7, v8, v9
	v_med3_f32 v8, v108, s64, v196
	v_med3_f32 v9, v109, s64, v196
	v_cvt_pk_fp8_f32 v7, v8, v9 op_sel:[0,0,1]
	v_med3_f32 v9, v102, s64, v196
	v_med3_f32 v11, v103, s64, v196
	v_cvt_pk_fp8_f32 v8, v9, v11
	v_med3_f32 v9, v104, s64, v196
	v_med3_f32 v11, v105, s64, v196
	v_cvt_pk_fp8_f32 v8, v9, v11 op_sel:[0,0,1]
	v_med3_f32 v11, v98, s64, v196
	v_med3_f32 v12, v99, s64, v196
	v_cvt_pk_fp8_f32 v9, v11, v12
	v_med3_f32 v11, v100, s64, v196
	v_med3_f32 v12, v101, s64, v196
	v_cvt_pk_fp8_f32 v9, v11, v12 op_sel:[0,0,1]
	v_add_u32_e32 v11, 0x10000, v10
	buffer_store_dwordx4 v[2:5], v11, s[4:7], 0 offen
	s_nop 1
	v_add_u32_e32 v2, 0x18000, v10
	buffer_store_dwordx4 v[6:9], v2, s[4:7], 0 offen
	s_nop 1
	v_med3_f32 v3, v94, s64, v196
	v_med3_f32 v4, v95, s64, v196
	v_cvt_pk_fp8_f32 v2, v3, v4
	v_med3_f32 v3, v96, s64, v196
	v_med3_f32 v4, v97, s64, v196
	v_cvt_pk_fp8_f32 v2, v3, v4 op_sel:[0,0,1]
	v_med3_f32 v4, v90, s64, v196
	v_med3_f32 v5, v91, s64, v196
	v_cvt_pk_fp8_f32 v3, v4, v5
	v_med3_f32 v4, v92, s64, v196
	v_med3_f32 v5, v93, s64, v196
	v_cvt_pk_fp8_f32 v3, v4, v5 op_sel:[0,0,1]
	v_med3_f32 v5, v86, s64, v196
	v_med3_f32 v6, v87, s64, v196
	v_cvt_pk_fp8_f32 v4, v5, v6
	v_med3_f32 v5, v88, s64, v196
	v_med3_f32 v6, v89, s64, v196
	v_cvt_pk_fp8_f32 v4, v5, v6 op_sel:[0,0,1]
	v_med3_f32 v6, v82, s64, v196
	v_med3_f32 v7, v83, s64, v196
	v_cvt_pk_fp8_f32 v5, v6, v7
	v_med3_f32 v6, v84, s64, v196
	v_med3_f32 v7, v85, s64, v196
	v_cvt_pk_fp8_f32 v5, v6, v7 op_sel:[0,0,1]
	v_med3_f32 v7, v78, s64, v196
	v_med3_f32 v8, v79, s64, v196
	v_cvt_pk_fp8_f32 v6, v7, v8
	v_med3_f32 v7, v80, s64, v196
	v_med3_f32 v8, v81, s64, v196
	v_cvt_pk_fp8_f32 v6, v7, v8 op_sel:[0,0,1]
	v_med3_f32 v8, v74, s64, v196
	v_med3_f32 v9, v75, s64, v196
	v_cvt_pk_fp8_f32 v7, v8, v9
	v_med3_f32 v8, v76, s64, v196
	v_med3_f32 v9, v77, s64, v196
	v_cvt_pk_fp8_f32 v7, v8, v9 op_sel:[0,0,1]
	v_med3_f32 v9, v70, s64, v196
	v_med3_f32 v11, v71, s64, v196
	v_cvt_pk_fp8_f32 v8, v9, v11
	v_med3_f32 v9, v72, s64, v196
	v_med3_f32 v11, v73, s64, v196
	v_cvt_pk_fp8_f32 v8, v9, v11 op_sel:[0,0,1]
	v_med3_f32 v11, v66, s64, v196
	v_med3_f32 v12, v67, s64, v196
	v_cvt_pk_fp8_f32 v9, v11, v12
	v_med3_f32 v11, v68, s64, v196
	v_med3_f32 v12, v69, s64, v196
	v_cvt_pk_fp8_f32 v9, v11, v12 op_sel:[0,0,1]
	v_add_u32_e32 v11, 0x40000, v10
	buffer_store_dwordx4 v[2:5], v11, s[4:7], 0 offen
	s_nop 1
	v_add_u32_e32 v2, 0x48000, v10
	buffer_store_dwordx4 v[6:9], v2, s[4:7], 0 offen
	s_nop 1
	v_med3_f32 v3, v62, s64, v196
	v_med3_f32 v4, v63, s64, v196
	v_cvt_pk_fp8_f32 v2, v3, v4
	v_med3_f32 v3, v64, s64, v196
	v_med3_f32 v4, v65, s64, v196
	v_cvt_pk_fp8_f32 v2, v3, v4 op_sel:[0,0,1]
	v_med3_f32 v4, v58, s64, v196
	v_med3_f32 v5, v59, s64, v196
	v_cvt_pk_fp8_f32 v3, v4, v5
	v_med3_f32 v4, v60, s64, v196
	v_med3_f32 v5, v61, s64, v196
	v_cvt_pk_fp8_f32 v3, v4, v5 op_sel:[0,0,1]
	v_med3_f32 v5, v54, s64, v196
	v_med3_f32 v6, v55, s64, v196
	v_cvt_pk_fp8_f32 v4, v5, v6
	v_med3_f32 v5, v56, s64, v196
	v_med3_f32 v6, v57, s64, v196
	v_cvt_pk_fp8_f32 v4, v5, v6 op_sel:[0,0,1]
	v_med3_f32 v6, v50, s64, v196
	v_med3_f32 v7, v51, s64, v196
	v_cvt_pk_fp8_f32 v5, v6, v7
	v_med3_f32 v6, v52, s64, v196
	v_med3_f32 v7, v53, s64, v196
	v_cvt_pk_fp8_f32 v5, v6, v7 op_sel:[0,0,1]
	v_med3_f32 v7, v46, s64, v196
	v_med3_f32 v8, v47, s64, v196
	v_cvt_pk_fp8_f32 v6, v7, v8
	v_med3_f32 v7, v48, s64, v196
	v_med3_f32 v8, v49, s64, v196
	v_cvt_pk_fp8_f32 v6, v7, v8 op_sel:[0,0,1]
	v_med3_f32 v8, v42, s64, v196
	v_med3_f32 v9, v43, s64, v196
	v_cvt_pk_fp8_f32 v7, v8, v9
	v_med3_f32 v8, v44, s64, v196
	v_med3_f32 v9, v45, s64, v196
	v_cvt_pk_fp8_f32 v7, v8, v9 op_sel:[0,0,1]
	v_med3_f32 v9, v38, s64, v196
	v_med3_f32 v11, v39, s64, v196
	v_cvt_pk_fp8_f32 v8, v9, v11
	v_med3_f32 v9, v40, s64, v196
	v_med3_f32 v11, v41, s64, v196
	v_cvt_pk_fp8_f32 v8, v9, v11 op_sel:[0,0,1]
	v_med3_f32 v11, v34, s64, v196
	v_med3_f32 v12, v35, s64, v196
	v_cvt_pk_fp8_f32 v9, v11, v12
	v_med3_f32 v11, v36, s64, v196
	v_med3_f32 v12, v37, s64, v196
	v_cvt_pk_fp8_f32 v9, v11, v12 op_sel:[0,0,1]
	v_add_u32_e32 v11, 0x50000, v10
	buffer_store_dwordx4 v[2:5], v11, s[4:7], 0 offen
	s_nop 1
	s_and_b64 vcc, exec, s[2:3]
	s_mov_b64 s[2:3], -1
	v_add_u32_e32 v2, 0x58000, v10
	buffer_store_dwordx4 v[6:9], v2, s[4:7], 0 offen
	s_mov_b32 s98, 1
	s_nop 1
	s_cbranch_vccnz .LBB0_1436
	s_andn2_b64 vcc, exec, s[14:15]
	s_cbranch_vccnz .LBB0_1435
	s_barrier
	s_branch .LBB0_1435
